# diff-attention: first MFMA of each stage placed behind 9 max-tree VALU ops (LDS latency of the first V fragment covered)
# baseline (speedup 1.0000x reference)
.Lattn_nobias0_a:
	v_max3_f32 v228, v160, v161, v162
	v_max3_f32 v229, v163, v164, v165
	v_max3_f32 v228, v228, v166, v167
	v_max3_f32 v229, v229, v168, v169
	v_max3_f32 v228, v228, v170, v171
	v_max3_f32 v229, v229, v172, v173
	v_max3_f32 v228, v228, v174, v175
	v_max3_f32 v229, v229, v176, v177
	v_max3_f32 v228, v228, v178, v179
	s_waitcnt lgkmcnt(4)
	v_mfma_f32_32x32x16_bf16 v[112:127], v[128:131], v[144:147], v[112:127]
	ds_read_b64_tr_b16 v[156:157], v215 offset:32768
	ds_read_b64_tr_b16 v[158:159], v215 offset:34816
	v_max3_f32 v229, v229, v180, v181
	v_max3_f32 v228, v228, v182, v183
	v_max3_f32 v229, v229, v184, v185
	v_max3_f32 v228, v228, v186, v187
	s_waitcnt lgkmcnt(4)
	v_mfma_f32_32x32x16_bf16 v[96:111], v[128:131], v[148:151], v[96:111]
	ds_read_b64_tr_b16 v[144:145], v212 offset:36864
	ds_read_b64_tr_b16 v[146:147], v212 offset:38912
	v_max3_f32 v229, v229, v188, v189
	v_max3_f32 v228, v228, v190, v191
	v_max_f32_e32 v228, v228, v229
	v_mov_b32_e32 v229, v228
	s_nop 1
	s_waitcnt lgkmcnt(4)
	v_mfma_f32_32x32x16_bf16 v[80:95], v[128:131], v[152:155], v[80:95]
	ds_read_b64_tr_b16 v[148:149], v213 offset:36864
	ds_read_b64_tr_b16 v[150:151], v213 offset:38912
	v_permlane32_swap_b32_e32 v228, v229
	v_max_f32_e32 v228, v228, v229
	v_add_f32_e32 v228, s49, v228
	v_sub_f32_e32 v229, v228, v226
	s_waitcnt lgkmcnt(4)
	v_mfma_f32_32x32x16_bf16 v[48:63], v[128:131], v[156:159], v[48:63]
	ds_read_b64_tr_b16 v[152:153], v214 offset:36864
	ds_read_b64_tr_b16 v[154:155], v214 offset:38912
	v_cmp_lt_f32_e32 vcc, 0x41000000, v229
	s_nop 1
	v_cndmask_b32_e32 v229, v226, v228, vcc
	v_sub_f32_e32 v228, v226, v229
	v_exp_f32_e32 v228, v228
	v_mov_b32_e32 v226, v229
	v_subrev_f32_e32 v229, s49, v229
	v_cmp_neq_f32_e32 vcc, 1.0, v228
	s_cbranch_vccz .Lattn_noresc0_a
	ds_write_b32 v239, v228
	ds_read_b128 v[192:195], v249
	ds_read_b128 v[196:199], v249 offset:32
	ds_read_b128 v[200:203], v249 offset:64
	ds_read_b128 v[204:207], v249 offset:96
	s_waitcnt lgkmcnt(3)
	v_pk_mul_f32 v[64:65], v[64:65], v[192:193]
	v_pk_mul_f32 v[66:67], v[66:67], v[194:195]
	v_pk_mul_f32 v[32:33], v[32:33], v[192:193]
	v_pk_mul_f32 v[34:35], v[34:35], v[194:195]
	v_pk_mul_f32 v[16:17], v[16:17], v[192:193]
	v_pk_mul_f32 v[18:19], v[18:19], v[194:195]
	v_pk_mul_f32 v[0:1], v[0:1], v[192:193]
	v_pk_mul_f32 v[2:3], v[2:3], v[194:195]
	s_waitcnt lgkmcnt(2)
	v_pk_mul_f32 v[68:69], v[68:69], v[196:197]
	v_pk_mul_f32 v[70:71], v[70:71], v[198:199]
	v_pk_mul_f32 v[36:37], v[36:37], v[196:197]
	v_pk_mul_f32 v[38:39], v[38:39], v[198:199]
	v_pk_mul_f32 v[20:21], v[20:21], v[196:197]
	v_pk_mul_f32 v[22:23], v[22:23], v[198:199]
	v_pk_mul_f32 v[4:5], v[4:5], v[196:197]
	v_pk_mul_f32 v[6:7], v[6:7], v[198:199]
	s_waitcnt lgkmcnt(1)
	v_pk_mul_f32 v[72:73], v[72:73], v[200:201]
	v_pk_mul_f32 v[74:75], v[74:75], v[202:203]
	v_pk_mul_f32 v[40:41], v[40:41], v[200:201]
	v_pk_mul_f32 v[42:43], v[42:43], v[202:203]
	v_pk_mul_f32 v[24:25], v[24:25], v[200:201]
	v_pk_mul_f32 v[26:27], v[26:27], v[202:203]
	v_pk_mul_f32 v[8:9], v[8:9], v[200:201]
	v_pk_mul_f32 v[10:11], v[10:11], v[202:203]
	s_waitcnt lgkmcnt(0)
	v_pk_mul_f32 v[76:77], v[76:77], v[204:205]
	v_pk_mul_f32 v[78:79], v[78:79], v[206:207]
	v_pk_mul_f32 v[44:45], v[44:45], v[204:205]
	v_pk_mul_f32 v[46:47], v[46:47], v[206:207]
	v_pk_mul_f32 v[28:29], v[28:29], v[204:205]
	v_pk_mul_f32 v[30:31], v[30:31], v[206:207]
	v_pk_mul_f32 v[12:13], v[12:13], v[204:205]
	v_pk_mul_f32 v[14:15], v[14:15], v[206:207]

.Lattn_nobias1_c:
	v_max3_f32 v228, v128, v129, v130
	v_max3_f32 v229, v131, v132, v133
	v_max3_f32 v228, v228, v134, v135
	v_max3_f32 v229, v229, v136, v137
	v_max3_f32 v228, v228, v138, v139
	s_add_i32 s17, s41, 1
	s_cmp_lt_u32 s17, s42
	s_cbranch_scc0 .Lattn_nok0_c
	s_add_u32 s18, s14, 0x68000
	s_addc_u32 s19, s15, 0
	v_lshl_add_u64 v[254:255], v[210:211], 0, s[18:19]
	s_add_i32 s17, s44, s48
	s_mov_b32 m0, s17
	s_nop 0
	global_load_lds_dwordx4 v[254:255], off
.Lattn_nok0_c:
	v_max3_f32 v229, v229, v140, v141
	v_max3_f32 v228, v228, v142, v143
	v_max3_f32 v229, v229, v144, v145
	s_waitcnt lgkmcnt(4)
	v_mfma_f32_32x32x16_bf16 v[64:79], v[160:163], v[176:179], v[64:79]
	ds_read_b64_tr_b16 v[188:189], v215 offset:32768
	ds_read_b64_tr_b16 v[190:191], v215 offset:34816
	v_max3_f32 v228, v228, v146, v147
	v_max3_f32 v229, v229, v148, v149
	s_cmp_lt_u32 s41, s42
	s_cbranch_scc0 .Lattn_nov0_c
	v_lshl_add_u64 v[254:255], v[218:219], 0, s[14:15]
	s_add_i32 s17, s44, s51
	s_add_i32 m0, s17, 0x8000
	s_nop 0
	global_load_lds_dwordx4 v[254:255], off
.Lattn_nov0_c:
	v_max3_f32 v228, v228, v150, v151
	v_max3_f32 v229, v229, v152, v153
	s_waitcnt lgkmcnt(4)
	v_mfma_f32_32x32x16_bf16 v[32:47], v[160:163], v[180:183], v[32:47]
	ds_read_b64_tr_b16 v[176:177], v212 offset:36864
	ds_read_b64_tr_b16 v[178:179], v212 offset:38912
	v_max3_f32 v228, v228, v154, v155
	v_max3_f32 v229, v229, v156, v157
	v_max3_f32 v228, v228, v158, v159
	s_add_i32 s17, s41, 1
	s_cmp_lt_u32 s17, s42
	s_cbranch_scc0 .Lattn_nok1_c
	s_add_u32 s18, s14, 0x68000
	s_addc_u32 s19, s15, 0
	v_lshl_add_u64 v[254:255], v[216:217], 0, s[18:19]
	s_add_i32 s17, s44, s48
	s_add_i32 m0, s17, 0x400
	s_nop 0
	global_load_lds_dwordx4 v[254:255], off
.Lattn_nok1_c:
	v_max_f32_e32 v228, v228, v229
	v_mov_b32_e32 v229, v228
	s_waitcnt lgkmcnt(4)
	v_mfma_f32_32x32x16_bf16 v[16:31], v[160:163], v[184:187], v[16:31]
	ds_read_b64_tr_b16 v[180:181], v213 offset:36864
	ds_read_b64_tr_b16 v[182:183], v213 offset:38912
	s_nop 1
	v_permlane32_swap_b32_e32 v228, v229
	v_max_f32_e32 v228, v228, v229
	s_cmp_lt_u32 s41, s42
	s_cbranch_scc0 .Lattn_nov1_c
	v_lshl_add_u64 v[254:255], v[220:221], 0, s[14:15]
	s_add_i32 s17, s44, s51
	s_add_i32 m0, s17, 0x8400
	s_nop 0
	global_load_lds_dwordx4 v[254:255], off
.Lattn_nov1_c:
	v_add_f32_e32 v228, s49, v228
	s_waitcnt lgkmcnt(4)
	v_mfma_f32_32x32x16_bf16 v[0:15], v[160:163], v[188:191], v[0:15]
	ds_read_b64_tr_b16 v[184:185], v214 offset:36864
	ds_read_b64_tr_b16 v[186:187], v214 offset:38912
	v_sub_f32_e32 v229, v228, v227
	v_cmp_lt_f32_e32 vcc, 0x41000000, v229
	s_nop 1
	v_cndmask_b32_e32 v229, v227, v228, vcc
	v_sub_f32_e32 v228, v227, v229
	v_exp_f32_e32 v228, v228
	v_mov_b32_e32 v227, v229
	v_subrev_f32_e32 v229, s49, v229
	v_cmp_neq_f32_e32 vcc, 1.0, v228
	s_cbranch_vccz .Lattn_noresc1_c
	ds_write_b32 v239, v228
	ds_read_b128 v[192:195], v249
	ds_read_b128 v[196:199], v249 offset:32
	ds_read_b128 v[200:203], v249 offset:64
	ds_read_b128 v[204:207], v249 offset:96
	s_waitcnt lgkmcnt(3)
	v_pk_mul_f32 v[112:113], v[112:113], v[192:193]
	v_pk_mul_f32 v[114:115], v[114:115], v[194:195]
	v_pk_mul_f32 v[96:97], v[96:97], v[192:193]
	v_pk_mul_f32 v[98:99], v[98:99], v[194:195]
	v_pk_mul_f32 v[80:81], v[80:81], v[192:193]
	v_pk_mul_f32 v[82:83], v[82:83], v[194:195]
	v_pk_mul_f32 v[48:49], v[48:49], v[192:193]
	v_pk_mul_f32 v[50:51], v[50:51], v[194:195]
	s_waitcnt lgkmcnt(2)
	v_pk_mul_f32 v[116:117], v[116:117], v[196:197]
	v_pk_mul_f32 v[118:119], v[118:119], v[198:199]
	v_pk_mul_f32 v[100:101], v[100:101], v[196:197]
	v_pk_mul_f32 v[102:103], v[102:103], v[198:199]
	v_pk_mul_f32 v[84:85], v[84:85], v[196:197]
	v_pk_mul_f32 v[86:87], v[86:87], v[198:199]
	v_pk_mul_f32 v[52:53], v[52:53], v[196:197]
	v_pk_mul_f32 v[54:55], v[54:55], v[198:199]
	s_waitcnt lgkmcnt(1)
	v_pk_mul_f32 v[120:121], v[120:121], v[200:201]
	v_pk_mul_f32 v[122:123], v[122:123], v[202:203]
	v_pk_mul_f32 v[104:105], v[104:105], v[200:201]
	v_pk_mul_f32 v[106:107], v[106:107], v[202:203]
	v_pk_mul_f32 v[88:89], v[88:89], v[200:201]
	v_pk_mul_f32 v[90:91], v[90:91], v[202:203]
	v_pk_mul_f32 v[56:57], v[56:57], v[200:201]
	v_pk_mul_f32 v[58:59], v[58:59], v[202:203]
	s_waitcnt lgkmcnt(0)
	v_pk_mul_f32 v[124:125], v[124:125], v[204:205]
	v_pk_mul_f32 v[126:127], v[126:127], v[206:207]
	v_pk_mul_f32 v[108:109], v[108:109], v[204:205]
	v_pk_mul_f32 v[110:111], v[110:111], v[206:207]
	v_pk_mul_f32 v[92:93], v[92:93], v[204:205]
	v_pk_mul_f32 v[94:95], v[94:95], v[206:207]
	v_pk_mul_f32 v[60:61], v[60:61], v[204:205]
	v_pk_mul_f32 v[62:63], v[62:63], v[206:207]
